# select matrices via exact packed-f16 integer arithmetic (34 instead of 45 VALU per pass); step head trimmed (saddr x gather, ds_read prefetch on the LDS fast path)
# speedup vs baseline: 1.0713x; 1.0052x over previous
.LBB1_143:
	s_or_b64 exec, exec, s[2:3]
	v_cndmask_b32_e64 v24, v14, 0, s[4:5]
	v_ashrrev_i32_e32 v25, 31, v24
	v_lshlrev_b64 v[24:25], 3, v[24:25]
	s_mov_b64 s[2:3], src_shared_base
	v_lshl_add_u64 v[24:25], s[56:57], 0, v[24:25]
	v_mov_b32_e32 v14, s3
	v_cndmask_b32_e64 v232, v24, 0, s[4:5]
	v_add_lshl_u32 v24, s13, v1, 1
	v_cndmask_b32_e64 v233, v25, v14, s[4:5]
	s_mov_b32 s81, s4
	v_ashrrev_i32_e32 v25, 31, v24
	v_lshl_add_u64 v[24:25], v[24:25], 2, v[232:233]
	flat_load_dwordx2 v[82:83], v[24:25]
	s_mov_b32 s2, 0x4038aa3b
	v_add_f32_e32 v239, s33, v11
	s_waitcnt vmcnt(0)
	v_fma_mixlo_f16 v11, v18, s2, 0
	v_fma_mixlo_f16 v25, v16, s2, 0
	v_fma_mixlo_f16 v27, v17, s2, 0
	v_add_lshl_u32 v22, s13, v22, 1
	v_fma_mixlo_f16 v14, v19, s2, 0
	v_fma_mixlo_f16 v18, v18, s2, -v11 op_sel_hi:[0,0,1]
	v_fma_mixlo_f16 v16, v16, s2, -v25 op_sel_hi:[0,0,1]
	v_fma_mixlo_f16 v17, v17, s2, -v27 op_sel_hi:[0,0,1]
	s_mov_b32 s14, 0x186a0
	v_ashrrev_i32_e32 v23, 31, v22
	v_fma_mixlo_f16 v19, v19, s2, -v14 op_sel_hi:[0,0,1]
	v_cndmask_b32_e64 v11, 0, v11, s[0:1]
	v_cndmask_b32_e64 v14, 0, v14, s[0:1]
	v_cndmask_b32_e64 v25, 0, v25, s[0:1]
	v_cndmask_b32_e64 v27, 0, v27, s[0:1]
	v_cndmask_b32_e64 v18, 0, v18, s[0:1]
	v_cndmask_b32_e64 v16, 0, v16, s[0:1]
	v_cndmask_b32_e64 v17, 0, v17, s[0:1]
	v_pack_b32_f16 v179, v11, v14
	v_pack_b32_f16 v178, v11, v18
	v_pack_b32_f16 v185, v27, v17
	v_pack_b32_f16 v182, v25, v16
	v_lshl_add_u64 v[16:17], v[22:23], 2, v[232:233]
	flat_load_dwordx2 v[236:237], v[16:17]
	v_mov_b32_e32 v17, v2
	v_cndmask_b32_e64 v19, 0, v19, s[0:1]
	v_pack_b32_f16 v180, v19, v14
	v_fma_mixlo_f16 v14, v13, s2, 0
	v_fma_mixlo_f16 v13, v13, s2, -v14 op_sel_hi:[0,0,1]
	v_cndmask_b32_e64 v14, 0, v14, s[0:1]
	v_cndmask_b32_e64 v13, 0, v13, s[0:1]
	v_fma_mixlo_f16 v24, v20, s2, 0
	v_fma_mixlo_f16 v26, v21, s2, 0
	v_or_b32_e32 v240, 64, v1
	v_pack_b32_f16 v188, v13, v14
	v_fma_mixlo_f16 v13, v10, s2, 0
	v_lshl_add_u32 v244, v1, 2, v3
	v_and_b32_e32 v0, 32, v0
	v_mov_b32_e32 v1, 0xa300
	v_fma_mixlo_f16 v20, v20, s2, -v24 op_sel_hi:[0,0,1]
	v_fma_mixlo_f16 v21, v21, s2, -v26 op_sel_hi:[0,0,1]
	v_fma_mixlo_f16 v10, v10, s2, -v13 op_sel_hi:[0,0,1]
	v_lshl_or_b32 v245, v0, 2, v1
	v_lshl_add_u32 v246, v8, 4, v1
	v_add_u32_e32 v3, 64, v7
	v_cndmask_b32_e64 v24, 0, v24, s[0:1]
	v_cndmask_b32_e64 v26, 0, v26, s[0:1]
	v_cndmask_b32_e64 v20, 0, v20, s[0:1]
	v_cndmask_b32_e64 v21, 0, v21, s[0:1]
	v_cndmask_b32_e64 v13, 0, v13, s[0:1]
	v_cndmask_b32_e64 v10, 0, v10, s[0:1]
	v_mov_b32_e32 v0, 0xc0
	v_pack_b32_f16 v183, v25, v26
	v_pack_b32_f16 v181, v24, v20
	v_pack_b32_f16 v184, v21, v26
	v_pack_b32_f16 v193, v13, v10
	v_lshlrev_b32_e32 v251, 3, v9
	v_mov_b32_e32 v7, v2
	v_mov_b32_e32 v9, v2
	v_mov_b32_e32 v10, v2
	v_mov_b32_e32 v13, v2
	v_add_u32_e32 v242, 8, v251
	s_waitcnt lgkmcnt(0)
	v_sub_u32_e32 v234, v231, v230
	s_mov_b64 s[4:5], 0
	v_mov_b32_e32 v249, s6
	v_mov_b32_e32 v231, s13
	s_mov_b32 s15, 0x5040100
	s_mov_b32 s73, 0x3c000000
	s_mov_b32 s74, 0x42004000
	s_mov_b32 s75, 0x48804800
	s_mov_b32 s76, 0x49804900
	s_mov_b32 s77, 0x4c404c00
	s_mov_b32 s78, 0x4cc04c80
	s_mov_b32 s79, 0x4e404e00
	s_mov_b32 s80, 0x4ec04e80
	v_mov_b32_e32 v197, 0x3c003c00
	s_mov_b32 s16, 0x10000
	s_mov_b32 s17, 0x7a100
	v_lshl_or_b32 v11, v82, 3, 3
	v_cmp_gt_u32_e32 vcc, s14, v82
	v_mov_b32_e32 v196, v83
	s_nop 0
	v_cndmask_b32_e32 v16, 3, v11, vcc
	v_lshl_add_u64 v[16:17], v[16:17], 2, s[54:55]
	global_load_dword v241, v[16:17], off
	v_fma_mixlo_f16 v11, v12, s2, 0
	v_fma_mixlo_f16 v12, v12, s2, -v11 op_sel_hi:[0,0,1]
	v_cndmask_b32_e64 v11, 0, v11, s[0:1]
	v_cndmask_b32_e64 v12, 0, v12, s[0:1]
	v_pack_b32_f16 v187, v11, v14
	v_pack_b32_f16 v186, v11, v12
	v_fma_mixlo_f16 v11, v4, s2, 0
	v_fma_mixlo_f16 v4, v4, s2, -v11 op_sel_hi:[0,0,1]
	v_cndmask_b32_e64 v11, 0, v11, s[0:1]
	v_cndmask_b32_e64 v4, 0, v4, s[0:1]
	v_fma_mixlo_f16 v16, v15, s2, 0
	v_pack_b32_f16 v190, v11, v4
	v_lshrrev_b32_e32 v4, 3, v8
	v_fma_mixlo_f16 v15, v15, s2, -v16 op_sel_hi:[0,0,1]
	v_fma_mixlo_f16 v12, v5, s2, 0
	v_and_b32_e32 v243, 4, v4
	v_cndmask_b32_e64 v16, 0, v16, s[0:1]
	v_cndmask_b32_e64 v15, 0, v15, s[0:1]
	v_fma_mixlo_f16 v5, v5, s2, -v12 op_sel_hi:[0,0,1]
	v_lshl_add_u32 v247, v243, 6, v1
	v_xor_b32_e32 v1, 32, v6
	v_pack_b32_f16 v189, v16, v15
	v_cndmask_b32_e64 v12, 0, v12, s[0:1]
	v_cndmask_b32_e64 v5, 0, v5, s[0:1]
	v_cmp_lt_i32_e32 vcc, v1, v3
	v_mov_b32_e32 v16, v2
	v_mov_b32_e32 v17, v2
	v_pack_b32_f16 v191, v11, v12
	v_pack_b32_f16 v192, v5, v12
	v_lshl_or_b32 v0, v4, 6, v0
	v_cndmask_b32_e32 v1, v6, v1, vcc
	v_mov_b32_e32 v3, v2
	v_mov_b32_e32 v4, v2
	v_mov_b32_e32 v5, v2
	v_mov_b32_e32 v6, v2
	v_mov_b32_e32 v8, v2
	v_mov_b32_e32 v11, v2
	v_mov_b32_e32 v12, v2
	v_mov_b32_e32 v14, v2
	v_mov_b32_e32 v15, v2
	v_mov_b64_e32 v[32:33], v[16:17]
	v_mov_b64_e32 v[48:49], v[16:17]
	v_mov_b64_e32 v[64:65], v[16:17]
	v_mov_b64_e32 v[80:81], v[16:17]
	v_lshlrev_b32_e32 v248, 2, v1
	v_add_u32_e32 v250, 0xa300, v0
	v_mov_b64_e32 v[30:31], v[14:15]
	v_mov_b64_e32 v[28:29], v[12:13]
	v_mov_b64_e32 v[26:27], v[10:11]
	v_mov_b64_e32 v[24:25], v[8:9]
	v_mov_b64_e32 v[22:23], v[6:7]
	v_mov_b64_e32 v[20:21], v[4:5]
	v_mov_b64_e32 v[18:19], v[2:3]
	v_mov_b64_e32 v[46:47], v[14:15]
	v_mov_b64_e32 v[44:45], v[12:13]
	v_mov_b64_e32 v[42:43], v[10:11]
	v_mov_b64_e32 v[40:41], v[8:9]
	v_mov_b64_e32 v[38:39], v[6:7]
	v_mov_b64_e32 v[36:37], v[4:5]
	v_mov_b64_e32 v[34:35], v[2:3]
	v_mov_b64_e32 v[62:63], v[14:15]
	v_mov_b64_e32 v[60:61], v[12:13]
	v_mov_b64_e32 v[58:59], v[10:11]
	v_mov_b64_e32 v[56:57], v[8:9]
	v_mov_b64_e32 v[54:55], v[6:7]
	v_mov_b64_e32 v[52:53], v[4:5]
	v_mov_b64_e32 v[50:51], v[2:3]
	v_mov_b64_e32 v[78:79], v[14:15]
	v_mov_b64_e32 v[76:77], v[12:13]
	v_mov_b64_e32 v[74:75], v[10:11]
	v_mov_b64_e32 v[72:73], v[8:9]
	v_mov_b64_e32 v[70:71], v[6:7]
	v_mov_b64_e32 v[68:69], v[4:5]
	v_mov_b64_e32 v[66:67], v[2:3]
	s_branch .LBB1_145

.LBB1_145:
	s_setprio 0
	s_waitcnt vmcnt(0)
	v_cvt_pk_f16_f32 v194, v241, v241
	v_lshl_or_b32 v4, v236, 5, 12
	v_cmp_gt_u32_e32 vcc, s14, v236
	v_cvt_f32_f16_e32 v3, v194
	v_sub_f32_e32 v3, v241, v3
	v_cvt_f16_f32_e32 v3, v3
	v_cndmask_b32_e32 v4, 12, v4, vcc
	v_perm_b32 v195, v196, v3, s15
	s_cmp_lg_u32 s81, 0
	s_cbranch_scc0 .Lslow_cs
	v_add_lshl_u32 v6, s13, v240, 3
	ds_read_b64 v[0:1], v6
.Lcs_done:
	global_load_dword v241, v4, s[54:55]
	s_add_i32 s18, s13, 32
	s_add_i32 s19, s13, 16
	s_mov_b64 s[6:7], 0
	v_mfma_f32_32x32x16_f16 v[82:97], v[194:197], v[178:181], 0
	v_mfma_f32_32x32x16_f16 v[98:113], v[194:197], v[182:185], 0
	v_add_u32_e32 v14, s13, v243
	v_sub_u32_e32 v3, v230, v14
	v_add_u32_e32 v4, v3, v234
	v_add_u32_e32 v5, -1, v3
	v_med3_i32 v4, v4, -1, 32
	v_med3_i32 v5, v5, -1, 32
	v_cvt_f32_i32_e32 v4, v4
	v_cvt_f32_i32_e32 v5, v5
	v_cvt_pk_f16_f32 v14, v4, v4
	v_cvt_pk_f16_f32 v15, v5, v5
	v_pk_add_f16 v3, v14, s73 neg_lo:[0,1] neg_hi:[0,1]
	v_pk_add_f16 v4, s73, v15 neg_lo:[0,1] neg_hi:[0,1]
	v_pk_min_f16 v6, v3, v4 clamp
	v_pk_add_f16 v5, v14, s74 neg_lo:[0,1] neg_hi:[0,1]
	v_pk_add_f16 v16, s74, v15 neg_lo:[0,1] neg_hi:[0,1]
	v_pk_min_f16 v7, v5, v16 clamp
	v_pk_add_f16 v3, v14, s75 neg_lo:[0,1] neg_hi:[0,1]
	v_pk_add_f16 v4, s75, v15 neg_lo:[0,1] neg_hi:[0,1]
	v_pk_min_f16 v8, v3, v4 clamp
	v_pk_add_f16 v5, v14, s76 neg_lo:[0,1] neg_hi:[0,1]
	v_pk_add_f16 v16, s76, v15 neg_lo:[0,1] neg_hi:[0,1]
	v_pk_min_f16 v9, v5, v16 clamp
	v_pk_add_f16 v3, v14, s77 neg_lo:[0,1] neg_hi:[0,1]
	v_pk_add_f16 v4, s77, v15 neg_lo:[0,1] neg_hi:[0,1]
	v_pk_min_f16 v10, v3, v4 clamp
	v_pk_add_f16 v5, v14, s78 neg_lo:[0,1] neg_hi:[0,1]
	v_pk_add_f16 v16, s78, v15 neg_lo:[0,1] neg_hi:[0,1]
	v_pk_min_f16 v11, v5, v16 clamp
	v_pk_add_f16 v3, v14, s79 neg_lo:[0,1] neg_hi:[0,1]
	v_pk_add_f16 v4, s79, v15 neg_lo:[0,1] neg_hi:[0,1]
	v_pk_min_f16 v12, v3, v4 clamp
	v_pk_add_f16 v5, v14, s80 neg_lo:[0,1] neg_hi:[0,1]
	v_pk_add_f16 v16, s80, v15 neg_lo:[0,1] neg_hi:[0,1]
	v_pk_min_f16 v13, v5, v16 clamp
	v_exp_f32_e32 v82, v82
	v_exp_f32_e32 v83, v83
	v_exp_f32_e32 v84, v84
	v_exp_f32_e32 v85, v85
	v_exp_f32_e32 v86, v86
	v_exp_f32_e32 v87, v87
	v_exp_f32_e32 v88, v88
	v_exp_f32_e32 v89, v89
	v_exp_f32_e32 v90, v90
	v_exp_f32_e32 v91, v91
	v_exp_f32_e32 v92, v92
	v_exp_f32_e32 v93, v93
	v_exp_f32_e32 v94, v94
	v_exp_f32_e32 v95, v95
	v_exp_f32_e32 v96, v96
	v_exp_f32_e32 v97, v97
	v_add_f32_e32 v82, 1.0, v82
	v_add_f32_e32 v83, 1.0, v83
	v_add_f32_e32 v84, 1.0, v84
	v_add_f32_e32 v85, 1.0, v85
	v_add_f32_e32 v86, 1.0, v86
	v_add_f32_e32 v87, 1.0, v87
	v_add_f32_e32 v88, 1.0, v88
	v_add_f32_e32 v89, 1.0, v89
	v_add_f32_e32 v90, 1.0, v90
	v_add_f32_e32 v91, 1.0, v91
	v_add_f32_e32 v92, 1.0, v92
	v_add_f32_e32 v93, 1.0, v93
	v_add_f32_e32 v94, 1.0, v94
	v_add_f32_e32 v95, 1.0, v95
	v_add_f32_e32 v96, 1.0, v96
	v_add_f32_e32 v97, 1.0, v97
	v_rcp_f32_e32 v82, v82
	v_rcp_f32_e32 v83, v83
	v_rcp_f32_e32 v84, v84
	v_rcp_f32_e32 v85, v85
	v_rcp_f32_e32 v86, v86
	v_rcp_f32_e32 v87, v87
	v_rcp_f32_e32 v88, v88
	v_rcp_f32_e32 v89, v89
	v_rcp_f32_e32 v90, v90
	v_rcp_f32_e32 v91, v91
	v_rcp_f32_e32 v92, v92
	v_rcp_f32_e32 v93, v93
	v_rcp_f32_e32 v94, v94
	v_rcp_f32_e32 v95, v95
	v_rcp_f32_e32 v96, v96
	v_rcp_f32_e32 v97, v97
	v_cvt_pk_f16_f32 v198, v82, v83
	v_cvt_pk_f16_f32 v199, v84, v85
	v_cvt_pk_f16_f32 v200, v86, v87
	v_cvt_pk_f16_f32 v201, v88, v89
	v_cvt_pk_f16_f32 v202, v90, v91
	v_cvt_pk_f16_f32 v203, v92, v93
	v_cvt_pk_f16_f32 v204, v94, v95
	v_cvt_pk_f16_f32 v205, v96, v97
	v_mfma_f32_32x32x16_f16 v[82:97], v[194:197], v[186:189], 0
	v_exp_f32_e32 v98, v98
	v_exp_f32_e32 v99, v99
	v_exp_f32_e32 v100, v100
	v_exp_f32_e32 v101, v101
	v_exp_f32_e32 v102, v102
	v_exp_f32_e32 v103, v103
	v_mfma_f32_32x32x16_f16 v[66:81], v[198:201], v[6:9], v[66:81]
	v_exp_f32_e32 v104, v104
	v_exp_f32_e32 v105, v105
	v_exp_f32_e32 v106, v106
	v_exp_f32_e32 v107, v107
	v_exp_f32_e32 v108, v108
	v_exp_f32_e32 v109, v109
	v_mfma_f32_32x32x16_f16 v[66:81], v[202:205], v[10:13], v[66:81]
	v_exp_f32_e32 v110, v110
	v_exp_f32_e32 v111, v111
	v_exp_f32_e32 v112, v112
	v_exp_f32_e32 v113, v113
	v_add_f32_e32 v98, 1.0, v98
	v_add_f32_e32 v99, 1.0, v99
	v_add_f32_e32 v100, 1.0, v100
	v_add_f32_e32 v101, 1.0, v101
	v_add_f32_e32 v102, 1.0, v102
	v_add_f32_e32 v103, 1.0, v103
	v_add_f32_e32 v104, 1.0, v104
	v_add_f32_e32 v105, 1.0, v105
	v_add_f32_e32 v106, 1.0, v106
	v_add_f32_e32 v107, 1.0, v107
	v_add_f32_e32 v108, 1.0, v108
	v_add_f32_e32 v109, 1.0, v109
	v_add_f32_e32 v110, 1.0, v110
	v_add_f32_e32 v111, 1.0, v111
	v_add_f32_e32 v112, 1.0, v112
	v_add_f32_e32 v113, 1.0, v113
	v_rcp_f32_e32 v98, v98
	v_rcp_f32_e32 v99, v99
	v_rcp_f32_e32 v100, v100
	v_rcp_f32_e32 v101, v101
	v_rcp_f32_e32 v102, v102
	v_rcp_f32_e32 v103, v103
	v_rcp_f32_e32 v104, v104
	v_rcp_f32_e32 v105, v105
	v_rcp_f32_e32 v106, v106
	v_rcp_f32_e32 v107, v107
	v_rcp_f32_e32 v108, v108
	v_rcp_f32_e32 v109, v109
	v_rcp_f32_e32 v110, v110
	v_rcp_f32_e32 v111, v111
	v_rcp_f32_e32 v112, v112
	v_rcp_f32_e32 v113, v113
	v_cvt_pk_f16_f32 v206, v98, v99
	v_cvt_pk_f16_f32 v207, v100, v101
	v_cvt_pk_f16_f32 v208, v102, v103
	v_cvt_pk_f16_f32 v209, v104, v105
	v_cvt_pk_f16_f32 v210, v106, v107
	v_cvt_pk_f16_f32 v211, v108, v109
	v_cvt_pk_f16_f32 v212, v110, v111
	v_cvt_pk_f16_f32 v213, v112, v113
	v_mfma_f32_32x32x16_f16 v[98:113], v[194:197], v[190:193], 0
	v_exp_f32_e32 v82, v82
	v_exp_f32_e32 v83, v83
	v_exp_f32_e32 v84, v84
	v_exp_f32_e32 v85, v85
	v_exp_f32_e32 v86, v86
	v_exp_f32_e32 v87, v87
	v_mfma_f32_32x32x16_f16 v[50:65], v[206:209], v[6:9], v[50:65]
	v_exp_f32_e32 v88, v88
	v_exp_f32_e32 v89, v89
	v_exp_f32_e32 v90, v90
	v_exp_f32_e32 v91, v91
	v_exp_f32_e32 v92, v92
	v_exp_f32_e32 v93, v93
	v_mfma_f32_32x32x16_f16 v[50:65], v[210:213], v[10:13], v[50:65]
	v_exp_f32_e32 v94, v94
	v_exp_f32_e32 v95, v95
	v_exp_f32_e32 v96, v96
	v_exp_f32_e32 v97, v97
	v_add_f32_e32 v82, 1.0, v82
	v_add_f32_e32 v83, 1.0, v83
	v_add_f32_e32 v84, 1.0, v84
	v_add_f32_e32 v85, 1.0, v85
	v_add_f32_e32 v86, 1.0, v86
	v_add_f32_e32 v87, 1.0, v87
	v_add_f32_e32 v88, 1.0, v88
	v_add_f32_e32 v89, 1.0, v89
	v_add_f32_e32 v90, 1.0, v90
	v_add_f32_e32 v91, 1.0, v91
	v_add_f32_e32 v92, 1.0, v92
	v_add_f32_e32 v93, 1.0, v93
	v_add_f32_e32 v94, 1.0, v94
	v_add_f32_e32 v95, 1.0, v95
	v_add_f32_e32 v96, 1.0, v96
	v_add_f32_e32 v97, 1.0, v97
	v_rcp_f32_e32 v82, v82
	v_rcp_f32_e32 v83, v83
	v_rcp_f32_e32 v84, v84
	v_rcp_f32_e32 v85, v85
	v_rcp_f32_e32 v86, v86
	v_rcp_f32_e32 v87, v87
	v_rcp_f32_e32 v88, v88
	v_rcp_f32_e32 v89, v89
	v_rcp_f32_e32 v90, v90
	v_rcp_f32_e32 v91, v91
	v_rcp_f32_e32 v92, v92
	v_rcp_f32_e32 v93, v93
	v_rcp_f32_e32 v94, v94
	v_rcp_f32_e32 v95, v95
	v_rcp_f32_e32 v96, v96
	v_rcp_f32_e32 v97, v97
	v_cvt_pk_f16_f32 v214, v82, v83
	v_cvt_pk_f16_f32 v215, v84, v85
	v_cvt_pk_f16_f32 v216, v86, v87
	v_cvt_pk_f16_f32 v217, v88, v89
	v_cvt_pk_f16_f32 v218, v90, v91
	v_cvt_pk_f16_f32 v219, v92, v93
	v_cvt_pk_f16_f32 v220, v94, v95
	v_cvt_pk_f16_f32 v221, v96, v97
	v_exp_f32_e32 v98, v98
	v_exp_f32_e32 v99, v99
	v_exp_f32_e32 v100, v100
	v_exp_f32_e32 v101, v101
	v_exp_f32_e32 v102, v102
	v_exp_f32_e32 v103, v103
	v_mfma_f32_32x32x16_f16 v[34:49], v[214:217], v[6:9], v[34:49]
	v_exp_f32_e32 v104, v104
	v_exp_f32_e32 v105, v105
	v_exp_f32_e32 v106, v106
	v_exp_f32_e32 v107, v107
	v_exp_f32_e32 v108, v108
	v_exp_f32_e32 v109, v109
	v_mfma_f32_32x32x16_f16 v[34:49], v[218:221], v[10:13], v[34:49]
	v_exp_f32_e32 v110, v110
	v_exp_f32_e32 v111, v111
	v_exp_f32_e32 v112, v112
	v_exp_f32_e32 v113, v113
	v_add_f32_e32 v98, 1.0, v98
	v_add_f32_e32 v99, 1.0, v99
	v_add_f32_e32 v100, 1.0, v100
	v_add_f32_e32 v101, 1.0, v101
	v_add_f32_e32 v102, 1.0, v102
	v_add_f32_e32 v103, 1.0, v103
	v_add_f32_e32 v104, 1.0, v104
	v_add_f32_e32 v105, 1.0, v105
	v_add_f32_e32 v106, 1.0, v106
	v_add_f32_e32 v107, 1.0, v107
	v_add_f32_e32 v108, 1.0, v108
	v_add_f32_e32 v109, 1.0, v109
	v_add_f32_e32 v110, 1.0, v110
	v_add_f32_e32 v111, 1.0, v111
	v_add_f32_e32 v112, 1.0, v112
	v_add_f32_e32 v113, 1.0, v113
	v_rcp_f32_e32 v98, v98
	v_rcp_f32_e32 v99, v99
	v_rcp_f32_e32 v100, v100
	v_rcp_f32_e32 v101, v101
	v_rcp_f32_e32 v102, v102
	v_rcp_f32_e32 v103, v103
	v_rcp_f32_e32 v104, v104
	v_rcp_f32_e32 v105, v105
	v_rcp_f32_e32 v106, v106
	v_rcp_f32_e32 v107, v107
	v_rcp_f32_e32 v108, v108
	v_rcp_f32_e32 v109, v109
	v_rcp_f32_e32 v110, v110
	v_rcp_f32_e32 v111, v111
	v_rcp_f32_e32 v112, v112
	v_rcp_f32_e32 v113, v113
	v_cvt_pk_f16_f32 v222, v98, v99
	v_cvt_pk_f16_f32 v223, v100, v101
	v_cvt_pk_f16_f32 v224, v102, v103
	v_cvt_pk_f16_f32 v225, v104, v105
	v_cvt_pk_f16_f32 v226, v106, v107
	v_cvt_pk_f16_f32 v227, v108, v109
	v_cvt_pk_f16_f32 v228, v110, v111
	v_cvt_pk_f16_f32 v229, v112, v113
	v_mfma_f32_32x32x16_f16 v[18:33], v[222:225], v[6:9], v[18:33]
	v_add_u32_e32 v194, s13, v243
	v_mfma_f32_32x32x16_f16 v[18:33], v[226:229], v[10:13], v[18:33]
	s_branch .Lpeel_join
.Lslow_cs:
	v_add_lshl_u32 v0, s13, v240, 1
	v_ashrrev_i32_e32 v1, 31, v0
	v_lshl_add_u64 v[6:7], v[0:1], 2, v[232:233]
	flat_load_dwordx2 v[0:1], v[6:7]
	s_branch .Lcs_done

.LBB1_149:
	v_sub_u32_e32 v3, v230, v194
	s_waitcnt lgkmcnt(0)
	v_add_u32_e32 v4, v3, v234
	v_add_u32_e32 v5, -1, v3
	v_med3_i32 v4, v4, -1, 32
	v_med3_i32 v5, v5, -1, 32
	v_cvt_f32_i32_e32 v4, v4
	v_cvt_f32_i32_e32 v5, v5
	v_cvt_pk_f16_f32 v14, v4, v4
	v_cvt_pk_f16_f32 v15, v5, v5
	v_cmp_gt_i32_e32 vcc, s19, v231
	v_cmp_lt_i32_e64 s[2:3], s13, v249
	s_and_b64 s[8:9], vcc, s[2:3]
	s_and_saveexec_b64 s[2:3], s[8:9]
	s_cbranch_execz .LBB1_151
	v_pk_add_f16 v3, v14, s73 neg_lo:[0,1] neg_hi:[0,1]
	v_pk_add_f16 v4, s73, v15 neg_lo:[0,1] neg_hi:[0,1]
	v_pk_min_f16 v6, v3, v4 clamp
	v_pk_add_f16 v5, v14, s74 neg_lo:[0,1] neg_hi:[0,1]
	v_pk_add_f16 v16, s74, v15 neg_lo:[0,1] neg_hi:[0,1]
	v_pk_min_f16 v7, v5, v16 clamp
	v_pk_add_f16 v3, v14, s75 neg_lo:[0,1] neg_hi:[0,1]
	v_pk_add_f16 v4, s75, v15 neg_lo:[0,1] neg_hi:[0,1]
	v_pk_min_f16 v8, v3, v4 clamp
	v_pk_add_f16 v5, v14, s76 neg_lo:[0,1] neg_hi:[0,1]
	v_pk_add_f16 v16, s76, v15 neg_lo:[0,1] neg_hi:[0,1]
	v_pk_min_f16 v9, v5, v16 clamp
	s_nop 1
	v_mfma_f32_32x32x16_f16 v[66:81], v[198:201], v[6:9], v[66:81]
	v_mfma_f32_32x32x16_f16 v[50:65], v[206:209], v[6:9], v[50:65]
	v_mfma_f32_32x32x16_f16 v[34:49], v[214:217], v[6:9], v[34:49]
	v_mfma_f32_32x32x16_f16 v[18:33], v[222:225], v[6:9], v[18:33]
.LBB1_151:
	s_or_b64 exec, exec, s[2:3]
	v_cmp_gt_i32_e32 vcc, s18, v231
	v_cmp_lt_i32_e64 s[2:3], s19, v249
	s_and_b64 s[8:9], vcc, s[2:3]
	s_and_saveexec_b64 s[2:3], s[8:9]
	s_cbranch_execz .LBB1_153
	v_pk_add_f16 v3, v14, s77 neg_lo:[0,1] neg_hi:[0,1]
	v_pk_add_f16 v4, s77, v15 neg_lo:[0,1] neg_hi:[0,1]
	v_pk_min_f16 v6, v3, v4 clamp
	v_pk_add_f16 v5, v14, s78 neg_lo:[0,1] neg_hi:[0,1]
	v_pk_add_f16 v16, s78, v15 neg_lo:[0,1] neg_hi:[0,1]
	v_pk_min_f16 v7, v5, v16 clamp
	v_pk_add_f16 v3, v14, s79 neg_lo:[0,1] neg_hi:[0,1]
	v_pk_add_f16 v4, s79, v15 neg_lo:[0,1] neg_hi:[0,1]
	v_pk_min_f16 v8, v3, v4 clamp
	v_pk_add_f16 v5, v14, s80 neg_lo:[0,1] neg_hi:[0,1]
	v_pk_add_f16 v16, s80, v15 neg_lo:[0,1] neg_hi:[0,1]
	v_pk_min_f16 v9, v5, v16 clamp
	s_nop 1
	v_mfma_f32_32x32x16_f16 v[66:81], v[202:205], v[6:9], v[66:81]
	v_mfma_f32_32x32x16_f16 v[50:65], v[210:213], v[6:9], v[50:65]
	v_mfma_f32_32x32x16_f16 v[34:49], v[218:221], v[6:9], v[34:49]
	v_mfma_f32_32x32x16_f16 v[18:33], v[226:229], v[6:9], v[18:33]

.Lpeel_join:
	v_cmp_ge_i32_e32 vcc, s18, v249
	s_mov_b64 s[8:9], 0
	s_and_saveexec_b64 s[2:3], vcc
	s_cbranch_execz .LBB1_148
	s_setprio 3
	v_cmp_gt_i32_e32 vcc, s12, v235
	s_and_b64 s[10:11], s[0:1], vcc
	ds_read_b128 v[82:85], v245 offset:32768
	ds_read_b128 v[86:89], v245 offset:32784
	ds_read_b128 v[90:93], v245 offset:32800
	ds_read_b128 v[94:97], v245 offset:32816
	ds_read_b128 v[98:101], v245 offset:32832
	ds_read_b128 v[102:105], v245 offset:32848
	ds_read_b128 v[106:109], v245 offset:32864
	ds_read_b128 v[110:113], v245 offset:32880
	ds_read_b128 v[114:117], v246 offset:0
	ds_read_b128 v[118:121], v246 offset:8192
	ds_read_b128 v[122:125], v246 offset:1024
	ds_read_b128 v[126:129], v246 offset:9216
	v_cvt_f32_i32_e32 v16, v234
	v_cvt_pk_f16_f32 v4, v66, v67
	v_cvt_pk_f16_f32 v5, v68, v69
	v_cvt_pk_f16_f32 v6, v70, v71
	v_cvt_pk_f16_f32 v7, v72, v73
	v_cvt_pk_f16_f32 v8, v74, v75
	v_cvt_pk_f16_f32 v9, v76, v77
	v_cvt_pk_f16_f32 v10, v78, v79
	v_cvt_pk_f16_f32 v11, v80, v81
	s_waitcnt lgkmcnt(8)
	v_pk_mul_f32 v[162:163], v[82:83], v[16:17] op_sel_hi:[1,0]
	v_pk_mul_f32 v[164:165], v[84:85], v[16:17] op_sel_hi:[1,0]
	v_pk_mul_f32 v[166:167], v[86:87], v[16:17] op_sel_hi:[1,0]
	v_pk_mul_f32 v[168:169], v[88:89], v[16:17] op_sel_hi:[1,0]
	v_pk_mul_f32 v[170:171], v[90:91], v[16:17] op_sel_hi:[1,0]
	v_pk_mul_f32 v[172:173], v[92:93], v[16:17] op_sel_hi:[1,0]
	v_pk_mul_f32 v[174:175], v[94:95], v[16:17] op_sel_hi:[1,0]
	v_pk_mul_f32 v[176:177], v[96:97], v[16:17] op_sel_hi:[1,0]
	ds_read_b128 v[130:133], v246 offset:2048
	ds_read_b128 v[134:137], v246 offset:10240
	ds_read_b128 v[138:141], v246 offset:3072
	ds_read_b128 v[142:145], v246 offset:11264
	s_waitcnt lgkmcnt(4)
	v_mfma_f32_32x32x16_f16 v[162:177], v[114:117], v[4:7], v[162:177]
	v_pk_mul_f32 v[146:147], v[98:99], v[16:17] op_sel_hi:[1,0]
	v_pk_mul_f32 v[148:149], v[100:101], v[16:17] op_sel_hi:[1,0]
	v_pk_mul_f32 v[150:151], v[102:103], v[16:17] op_sel_hi:[1,0]
	v_pk_mul_f32 v[152:153], v[104:105], v[16:17] op_sel_hi:[1,0]
	v_pk_mul_f32 v[154:155], v[106:107], v[16:17] op_sel_hi:[1,0]
	v_pk_mul_f32 v[156:157], v[108:109], v[16:17] op_sel_hi:[1,0]
	v_pk_mul_f32 v[158:159], v[110:111], v[16:17] op_sel_hi:[1,0]
	v_pk_mul_f32 v[160:161], v[112:113], v[16:17] op_sel_hi:[1,0]
	s_nop 1
	v_mfma_f32_32x32x16_f16 v[146:161], v[118:121], v[4:7], v[146:161]
	v_cvt_pk_f16_f32 v12, v50, v51
	v_cvt_pk_f16_f32 v13, v52, v53
	v_cvt_pk_f16_f32 v14, v54, v55
	v_cvt_pk_f16_f32 v15, v56, v57
	v_mfma_f32_32x32x16_f16 v[162:177], v[122:125], v[8:11], v[162:177]
	v_cvt_pk_f16_f32 v252, v58, v59
	v_cvt_pk_f16_f32 v253, v60, v61
	v_cvt_pk_f16_f32 v254, v62, v63
	v_cvt_pk_f16_f32 v255, v64, v65
	v_mfma_f32_32x32x16_f16 v[146:161], v[126:129], v[8:11], v[146:161]
	ds_read_b128 v[82:85], v246 offset:4096
	ds_read_b128 v[86:89], v246 offset:12288
	ds_read_b128 v[90:93], v246 offset:5120
	ds_read_b128 v[94:97], v246 offset:13312
	s_waitcnt lgkmcnt(4)
	v_mfma_f32_32x32x16_f16 v[162:177], v[130:133], v[12:15], v[162:177]
	v_cvt_pk_f16_f32 v4, v34, v35
	v_cvt_pk_f16_f32 v5, v36, v37
	v_mfma_f32_32x32x16_f16 v[146:161], v[134:137], v[12:15], v[146:161]
	v_cvt_pk_f16_f32 v6, v38, v39
	v_cvt_pk_f16_f32 v7, v40, v41
	v_mfma_f32_32x32x16_f16 v[162:177], v[138:141], v[252:255], v[162:177]
	v_cvt_pk_f16_f32 v8, v42, v43
	v_cvt_pk_f16_f32 v9, v44, v45
	v_mfma_f32_32x32x16_f16 v[146:161], v[142:145], v[252:255], v[146:161]
	v_cvt_pk_f16_f32 v10, v46, v47
	v_cvt_pk_f16_f32 v11, v48, v49
	ds_read_b128 v[98:101], v246 offset:6144
	ds_read_b128 v[102:105], v246 offset:14336
	ds_read_b128 v[106:109], v246 offset:7168
	ds_read_b128 v[110:113], v246 offset:15360
	s_waitcnt lgkmcnt(4)
	v_mfma_f32_32x32x16_f16 v[162:177], v[82:85], v[4:7], v[162:177]
	v_cvt_pk_f16_f32 v12, v18, v19
	v_cvt_pk_f16_f32 v13, v20, v21
	v_mfma_f32_32x32x16_f16 v[146:161], v[86:89], v[4:7], v[146:161]
	v_cvt_pk_f16_f32 v14, v22, v23
	v_cvt_pk_f16_f32 v15, v24, v25
	v_mfma_f32_32x32x16_f16 v[162:177], v[90:93], v[8:11], v[162:177]
	v_cvt_pk_f16_f32 v252, v26, v27
	v_cvt_pk_f16_f32 v253, v28, v29
	v_mfma_f32_32x32x16_f16 v[146:161], v[94:97], v[8:11], v[146:161]
	v_cvt_pk_f16_f32 v254, v30, v31
	v_cvt_pk_f16_f32 v255, v32, v33
	ds_read_b128 v[18:21], v246 offset:16384
	ds_read_b128 v[22:25], v246 offset:17408
	ds_read_b128 v[26:29], v246 offset:18432
	ds_read_b128 v[30:33], v246 offset:19456
	s_waitcnt lgkmcnt(4)
	v_mfma_f32_32x32x16_f16 v[162:177], v[98:101], v[12:15], v[162:177]
	v_mfma_f32_32x32x16_f16 v[146:161], v[102:105], v[12:15], v[146:161]
	v_mfma_f32_32x32x16_f16 v[162:177], v[106:109], v[252:255], v[162:177]
	v_mfma_f32_32x32x16_f16 v[146:161], v[110:113], v[252:255], v[146:161]
	ds_read_b128 v[130:133], v247 offset:33024
	ds_read_b128 v[134:137], v247 offset:33040
	ds_read_b128 v[138:141], v247 offset:33056
	ds_read_b128 v[142:145], v247 offset:33072
	ds_read_b128 v[114:117], v247 offset:33088
	ds_read_b128 v[118:121], v247 offset:33104
	ds_read_b128 v[122:125], v247 offset:33120
	ds_read_b128 v[126:129], v247 offset:33136
	s_nop 2
	v_cvt_pk_f16_f32 v4, v162, v163
	v_cvt_pk_f16_f32 v5, v164, v165
	v_cvt_pk_f16_f32 v6, v166, v167
	v_cvt_pk_f16_f32 v7, v168, v169
	v_cvt_pk_f16_f32 v8, v170, v171
	v_cvt_pk_f16_f32 v9, v172, v173
	v_cvt_pk_f16_f32 v10, v174, v175
	v_cvt_pk_f16_f32 v11, v176, v177
	v_cvt_pk_f16_f32 v12, v146, v147
	v_cvt_pk_f16_f32 v13, v148, v149
	v_cvt_pk_f16_f32 v14, v150, v151
	v_cvt_pk_f16_f32 v15, v152, v153
	v_cvt_pk_f16_f32 v252, v154, v155
	v_cvt_pk_f16_f32 v253, v156, v157
	v_cvt_pk_f16_f32 v254, v158, v159
	v_cvt_pk_f16_f32 v255, v160, v161
	s_waitcnt lgkmcnt(4)
	ds_read_b128 v[34:37], v246 offset:20480
	ds_read_b128 v[38:41], v246 offset:21504
	ds_read_b128 v[42:45], v246 offset:22528
	ds_read_b128 v[46:49], v246 offset:23552
	v_mfma_f32_32x32x16_f16 v[130:145], v[18:21], v[4:7], v[130:145]
	v_mfma_f32_32x32x16_f16 v[130:145], v[22:25], v[8:11], v[130:145]
	v_mfma_f32_32x32x16_f16 v[130:145], v[26:29], v[12:15], v[130:145]
	v_mfma_f32_32x32x16_f16 v[130:145], v[30:33], v[252:255], v[130:145]
	ds_read_b128 v[146:149], v247 offset:33536
	ds_read_b128 v[150:153], v247 offset:33552
	ds_read_b128 v[154:157], v247 offset:33568
	ds_read_b128 v[158:161], v247 offset:33584
	s_waitcnt lgkmcnt(4)
	ds_read_b128 v[98:101], v247 offset:33152
	ds_read_b128 v[102:105], v247 offset:33168
	ds_read_b128 v[106:109], v247 offset:33184
	ds_read_b128 v[110:113], v247 offset:33200
	ds_read_b128 v[50:53], v246 offset:24576
	ds_read_b128 v[54:57], v246 offset:25600
	ds_read_b128 v[58:61], v246 offset:26624
	ds_read_b128 v[62:65], v246 offset:27648
	v_mfma_f32_32x32x16_f16 v[114:129], v[34:37], v[4:7], v[114:129]
	v_exp_f32_e32 v130, v130
	v_exp_f32_e32 v131, v131
	v_exp_f32_e32 v132, v132
	v_exp_f32_e32 v133, v133
	v_exp_f32_e32 v134, v134
	v_exp_f32_e32 v135, v135
	v_exp_f32_e32 v136, v136
	v_exp_f32_e32 v137, v137
	v_mfma_f32_32x32x16_f16 v[114:129], v[38:41], v[8:11], v[114:129]
	v_exp_f32_e32 v138, v138
	v_exp_f32_e32 v139, v139
	v_exp_f32_e32 v140, v140
	v_exp_f32_e32 v141, v141
	v_exp_f32_e32 v142, v142
	v_exp_f32_e32 v143, v143
	v_exp_f32_e32 v144, v144
	v_exp_f32_e32 v145, v145
	v_mfma_f32_32x32x16_f16 v[114:129], v[42:45], v[12:15], v[114:129]
	v_add_f32_e32 v130, 1.0, v130
	v_add_f32_e32 v131, 1.0, v131
	v_add_f32_e32 v132, 1.0, v132
	v_add_f32_e32 v133, 1.0, v133
	v_add_f32_e32 v134, 1.0, v134
	v_add_f32_e32 v135, 1.0, v135
	v_add_f32_e32 v136, 1.0, v136
	v_add_f32_e32 v137, 1.0, v137
	v_add_f32_e32 v138, 1.0, v138
	v_add_f32_e32 v139, 1.0, v139
	v_add_f32_e32 v140, 1.0, v140
	v_add_f32_e32 v141, 1.0, v141
	v_add_f32_e32 v142, 1.0, v142
	v_add_f32_e32 v143, 1.0, v143
	v_add_f32_e32 v144, 1.0, v144
	v_add_f32_e32 v145, 1.0, v145
	v_mfma_f32_32x32x16_f16 v[114:129], v[46:49], v[252:255], v[114:129]
	v_rcp_f32_e32 v130, v130
	v_rcp_f32_e32 v131, v131
	v_rcp_f32_e32 v132, v132
	v_rcp_f32_e32 v133, v133
	v_rcp_f32_e32 v134, v134
	v_rcp_f32_e32 v135, v135
	v_rcp_f32_e32 v136, v136
	v_rcp_f32_e32 v137, v137
	v_rcp_f32_e32 v138, v138
	v_rcp_f32_e32 v139, v139
	v_rcp_f32_e32 v140, v140
	v_rcp_f32_e32 v141, v141
	v_rcp_f32_e32 v142, v142
	v_rcp_f32_e32 v143, v143
	v_rcp_f32_e32 v144, v144
	v_rcp_f32_e32 v145, v145
	s_waitcnt lgkmcnt(8)
	ds_read_b128 v[162:165], v247 offset:33600
	ds_read_b128 v[166:169], v247 offset:33616
	ds_read_b128 v[170:173], v247 offset:33632
	ds_read_b128 v[174:177], v247 offset:33648
	v_mul_f32_e32 v3, v146, v130
	v_mul_f32_e32 v16, v147, v131
	v_mul_f32_e32 v17, v148, v132
	v_fmac_f32_e32 v3, v149, v133
	v_fmac_f32_e32 v16, v150, v134
	v_fmac_f32_e32 v17, v151, v135
	v_fmac_f32_e32 v3, v152, v136
	v_fmac_f32_e32 v16, v153, v137
	v_fmac_f32_e32 v17, v154, v138
	v_fmac_f32_e32 v3, v155, v139
	v_fmac_f32_e32 v16, v156, v140
	v_fmac_f32_e32 v17, v157, v141
	v_fmac_f32_e32 v3, v158, v142
	v_fmac_f32_e32 v16, v159, v143
	v_fmac_f32_e32 v17, v160, v144
	v_fmac_f32_e32 v3, v161, v145
	s_waitcnt lgkmcnt(4)
	ds_read_b128 v[82:85], v247 offset:33216
	ds_read_b128 v[86:89], v247 offset:33232
	ds_read_b128 v[90:93], v247 offset:33248
	ds_read_b128 v[94:97], v247 offset:33264
	ds_read_b128 v[66:69], v246 offset:28672
	ds_read_b128 v[70:73], v246 offset:29696
	ds_read_b128 v[74:77], v246 offset:30720
	ds_read_b128 v[78:81], v246 offset:31744
	v_mfma_f32_32x32x16_f16 v[98:113], v[50:53], v[4:7], v[98:113]
	v_exp_f32_e32 v114, v114
	v_exp_f32_e32 v115, v115
	v_exp_f32_e32 v116, v116
	v_exp_f32_e32 v117, v117
	v_exp_f32_e32 v118, v118
	v_exp_f32_e32 v119, v119
	v_exp_f32_e32 v120, v120
	v_exp_f32_e32 v121, v121
	v_mfma_f32_32x32x16_f16 v[98:113], v[54:57], v[8:11], v[98:113]
	v_exp_f32_e32 v122, v122
	v_exp_f32_e32 v123, v123
	v_exp_f32_e32 v124, v124
	v_exp_f32_e32 v125, v125
	v_exp_f32_e32 v126, v126
	v_exp_f32_e32 v127, v127
	v_exp_f32_e32 v128, v128
	v_exp_f32_e32 v129, v129
	v_mfma_f32_32x32x16_f16 v[98:113], v[58:61], v[12:15], v[98:113]
	v_add_f32_e32 v114, 1.0, v114
	v_add_f32_e32 v115, 1.0, v115
	v_add_f32_e32 v116, 1.0, v116
	v_add_f32_e32 v117, 1.0, v117
	v_add_f32_e32 v118, 1.0, v118
	v_add_f32_e32 v119, 1.0, v119
	v_add_f32_e32 v120, 1.0, v120
	v_add_f32_e32 v121, 1.0, v121
	v_add_f32_e32 v122, 1.0, v122
	v_add_f32_e32 v123, 1.0, v123
	v_add_f32_e32 v124, 1.0, v124
	v_add_f32_e32 v125, 1.0, v125
	v_add_f32_e32 v126, 1.0, v126
	v_add_f32_e32 v127, 1.0, v127
	v_add_f32_e32 v128, 1.0, v128
	v_add_f32_e32 v129, 1.0, v129
	v_mfma_f32_32x32x16_f16 v[98:113], v[62:65], v[252:255], v[98:113]
	v_rcp_f32_e32 v114, v114
	v_rcp_f32_e32 v115, v115
	v_rcp_f32_e32 v116, v116
	v_rcp_f32_e32 v117, v117
	v_rcp_f32_e32 v118, v118
	v_rcp_f32_e32 v119, v119
	v_rcp_f32_e32 v120, v120
	v_rcp_f32_e32 v121, v121
	v_rcp_f32_e32 v122, v122
	v_rcp_f32_e32 v123, v123
	v_rcp_f32_e32 v124, v124
	v_rcp_f32_e32 v125, v125
	v_rcp_f32_e32 v126, v126
	v_rcp_f32_e32 v127, v127
	v_rcp_f32_e32 v128, v128
	v_rcp_f32_e32 v129, v129
	s_waitcnt lgkmcnt(8)
	ds_read_b128 v[18:21], v247 offset:33664
	ds_read_b128 v[22:25], v247 offset:33680
	ds_read_b128 v[26:29], v247 offset:33696
	ds_read_b128 v[30:33], v247 offset:33712
	v_fmac_f32_e32 v3, v162, v114
	v_fmac_f32_e32 v16, v163, v115
	v_fmac_f32_e32 v17, v164, v116
	v_fmac_f32_e32 v3, v165, v117
	v_fmac_f32_e32 v16, v166, v118
	v_fmac_f32_e32 v17, v167, v119
	v_fmac_f32_e32 v3, v168, v120
	v_fmac_f32_e32 v16, v169, v121
	v_fmac_f32_e32 v17, v170, v122
	v_fmac_f32_e32 v3, v171, v123
	v_fmac_f32_e32 v16, v172, v124
	v_fmac_f32_e32 v17, v173, v125
	v_fmac_f32_e32 v3, v174, v126
	v_fmac_f32_e32 v16, v175, v127
	v_fmac_f32_e32 v17, v176, v128
	v_fmac_f32_e32 v3, v177, v129
	s_waitcnt lgkmcnt(4)
	ds_read_b128 v[146:149], v247 offset:33728
	ds_read_b128 v[150:153], v247 offset:33744
	ds_read_b128 v[154:157], v247 offset:33760
	ds_read_b128 v[158:161], v247 offset:33776
	v_mfma_f32_32x32x16_f16 v[82:97], v[66:69], v[4:7], v[82:97]
	v_exp_f32_e32 v98, v98
	v_exp_f32_e32 v99, v99
	v_exp_f32_e32 v100, v100
	v_exp_f32_e32 v101, v101
	v_exp_f32_e32 v102, v102
	v_exp_f32_e32 v103, v103
	v_exp_f32_e32 v104, v104
	v_exp_f32_e32 v105, v105
	v_mfma_f32_32x32x16_f16 v[82:97], v[70:73], v[8:11], v[82:97]
	v_exp_f32_e32 v106, v106
	v_exp_f32_e32 v107, v107
	v_exp_f32_e32 v108, v108
	v_exp_f32_e32 v109, v109
	v_exp_f32_e32 v110, v110
	v_exp_f32_e32 v111, v111
	v_exp_f32_e32 v112, v112
	v_exp_f32_e32 v113, v113
	v_mfma_f32_32x32x16_f16 v[82:97], v[74:77], v[12:15], v[82:97]
	v_add_f32_e32 v98, 1.0, v98
	v_add_f32_e32 v99, 1.0, v99
	v_add_f32_e32 v100, 1.0, v100
	v_add_f32_e32 v101, 1.0, v101
	v_add_f32_e32 v102, 1.0, v102
	v_add_f32_e32 v103, 1.0, v103
	v_add_f32_e32 v104, 1.0, v104
	v_add_f32_e32 v105, 1.0, v105
	v_add_f32_e32 v106, 1.0, v106
	v_add_f32_e32 v107, 1.0, v107
	v_add_f32_e32 v108, 1.0, v108
	v_add_f32_e32 v109, 1.0, v109
	v_add_f32_e32 v110, 1.0, v110
	v_add_f32_e32 v111, 1.0, v111
	v_add_f32_e32 v112, 1.0, v112
	v_add_f32_e32 v113, 1.0, v113
	v_mfma_f32_32x32x16_f16 v[82:97], v[78:81], v[252:255], v[82:97]
	v_rcp_f32_e32 v98, v98
	v_rcp_f32_e32 v99, v99
	v_rcp_f32_e32 v100, v100
	v_rcp_f32_e32 v101, v101
	v_rcp_f32_e32 v102, v102
	v_rcp_f32_e32 v103, v103
	v_rcp_f32_e32 v104, v104
	v_rcp_f32_e32 v105, v105
	v_rcp_f32_e32 v106, v106
	v_rcp_f32_e32 v107, v107
	v_rcp_f32_e32 v108, v108
	v_rcp_f32_e32 v109, v109
	v_rcp_f32_e32 v110, v110
	v_rcp_f32_e32 v111, v111
	v_rcp_f32_e32 v112, v112
	v_rcp_f32_e32 v113, v113
	s_waitcnt lgkmcnt(4)
	v_fmac_f32_e32 v3, v18, v98
	v_fmac_f32_e32 v16, v19, v99
	v_fmac_f32_e32 v17, v20, v100
	v_fmac_f32_e32 v3, v21, v101
	v_fmac_f32_e32 v16, v22, v102
	v_fmac_f32_e32 v17, v23, v103
	v_fmac_f32_e32 v3, v24, v104
	v_fmac_f32_e32 v16, v25, v105
	v_fmac_f32_e32 v17, v26, v106
	v_fmac_f32_e32 v3, v27, v107
	v_fmac_f32_e32 v16, v28, v108
	v_fmac_f32_e32 v17, v29, v109
	v_fmac_f32_e32 v3, v30, v110
	v_fmac_f32_e32 v16, v31, v111
	v_fmac_f32_e32 v17, v32, v112
	v_fmac_f32_e32 v3, v33, v113
	v_mov_b32_e32 v4, 0
	v_mov_b32_e32 v5, 0
	v_mov_b32_e32 v6, 0
	v_mov_b32_e32 v7, 0
	v_exp_f32_e32 v82, v82
	v_exp_f32_e32 v83, v83
	v_exp_f32_e32 v84, v84
	v_exp_f32_e32 v85, v85
	v_exp_f32_e32 v86, v86
	v_exp_f32_e32 v87, v87
	v_exp_f32_e32 v88, v88
	v_exp_f32_e32 v89, v89
	v_mfma_f32_32x32x16_f16 v[66:81], v[4:7], v[4:7], 0
	v_exp_f32_e32 v90, v90
	v_exp_f32_e32 v91, v91
	v_exp_f32_e32 v92, v92
	v_exp_f32_e32 v93, v93
	v_exp_f32_e32 v94, v94
	v_exp_f32_e32 v95, v95
	v_exp_f32_e32 v96, v96
	v_exp_f32_e32 v97, v97
	v_mfma_f32_32x32x16_f16 v[50:65], v[4:7], v[4:7], 0
	v_add_f32_e32 v82, 1.0, v82
	v_add_f32_e32 v83, 1.0, v83
	v_add_f32_e32 v84, 1.0, v84
	v_add_f32_e32 v85, 1.0, v85
	v_add_f32_e32 v86, 1.0, v86
	v_add_f32_e32 v87, 1.0, v87
	v_add_f32_e32 v88, 1.0, v88
	v_add_f32_e32 v89, 1.0, v89
	v_add_f32_e32 v90, 1.0, v90
	v_add_f32_e32 v91, 1.0, v91
	v_add_f32_e32 v92, 1.0, v92
	v_add_f32_e32 v93, 1.0, v93
	v_add_f32_e32 v94, 1.0, v94
	v_add_f32_e32 v95, 1.0, v95
	v_add_f32_e32 v96, 1.0, v96
	v_add_f32_e32 v97, 1.0, v97
	v_mfma_f32_32x32x16_f16 v[34:49], v[4:7], v[4:7], 0
	v_rcp_f32_e32 v82, v82
	v_rcp_f32_e32 v83, v83
	v_rcp_f32_e32 v84, v84
	v_rcp_f32_e32 v85, v85
	v_rcp_f32_e32 v86, v86
	v_rcp_f32_e32 v87, v87
	v_rcp_f32_e32 v88, v88
	v_rcp_f32_e32 v89, v89
	v_rcp_f32_e32 v90, v90
	v_rcp_f32_e32 v91, v91
	v_rcp_f32_e32 v92, v92
	v_rcp_f32_e32 v93, v93
	v_rcp_f32_e32 v94, v94
	v_rcp_f32_e32 v95, v95
	v_rcp_f32_e32 v96, v96
	v_rcp_f32_e32 v97, v97
	s_waitcnt lgkmcnt(0)
	v_mfma_f32_32x32x16_f16 v[18:33], v[4:7], v[4:7], 0
	v_fmac_f32_e32 v3, v146, v82
	v_fmac_f32_e32 v16, v147, v83
	v_fmac_f32_e32 v17, v148, v84
	v_fmac_f32_e32 v3, v149, v85
	v_fmac_f32_e32 v16, v150, v86
	v_fmac_f32_e32 v17, v151, v87
	v_fmac_f32_e32 v3, v152, v88
	v_fmac_f32_e32 v16, v153, v89
	v_fmac_f32_e32 v17, v154, v90
	v_fmac_f32_e32 v3, v155, v91
	v_fmac_f32_e32 v16, v156, v92
	v_fmac_f32_e32 v17, v157, v93
	v_fmac_f32_e32 v3, v158, v94
	v_fmac_f32_e32 v16, v159, v95
	v_fmac_f32_e32 v17, v160, v96
	v_fmac_f32_e32 v3, v161, v97
	v_add_f32_e32 v3, v3, v16
	v_add_f32_e32 v3, v3, v17
	v_mov_b32_e32 v4, v3
	s_nop 1
	v_permlane32_swap_b32_e32 v4, v3
	s_and_saveexec_b64 s[8:9], s[10:11]
	s_cbranch_execz .LBB1_156
	s_waitcnt vmcnt(0)
	v_mul_f32_e32 v5, 0x40549a78, v238
	v_exp_f32_e32 v5, v5
	v_add_f32_e32 v3, v3, v4
	v_ashrrev_i32_e32 v7, 31, v235
	v_mov_b32_e32 v6, v235
	v_add_f32_e32 v3, v239, v3
	v_lshl_add_u64 v[6:7], v[6:7], 2, s[52:53]
	v_mul_f32_e32 v3, v5, v3
	global_store_dword v[6:7], v3, off
